# MoBA-layer QKV GEMM phases: every second workgroup of an XCD starts ~4 us late (s_sleep) so the two halves output store bursts interleave
# speedup vs baseline: 1.0037x; 1.0037x over previous
.LBB0_225:
	s_add_u32 s4, s90, 0x300000
	s_addc_u32 s5, s91, 0
	s_cmp_lt_i32 s12, 2
	s_cselect_b64 s[0:1], -1, 0
	s_cmp_gt_i32 s13, 1
	s_cselect_b64 s[2:3], -1, 0
	s_and_b64 s[0:1], s[0:1], s[2:3]
	s_andn2_b64 vcc, exec, s[0:1]
	s_cbranch_vccnz .LBB0_301
	v_readlane_b32 s32, v254, 0
	s_nop 3
	s_bitcmp1_b32 s32, 3
	s_cbranch_scc0 .Lstag_0
	s_sleep 127

.LBB0_2920:
	s_cmp_gt_i32 s12, 39
	s_cselect_b64 s[0:1], -1, 0
	s_cmp_lt_i32 s13, 31
	s_cselect_b64 s[2:3], -1, 0
	s_or_b64 s[0:1], s[0:1], s[2:3]
	s_and_b64 vcc, exec, s[0:1]
	v_readlane_b32 s83, v254, 0
	s_cbranch_vccnz .LBB0_3660
	s_add_u32 s0, s90, 0x380000
	s_mov_b64 s[84:85], s[12:13]
	s_addc_u32 s1, s91, 0
	s_cmp_lt_i32 s84, 32
	s_cselect_b64 s[2:3], -1, 0
	s_cmp_gt_u32 s85, 31
	s_cselect_b64 s[4:5], -1, 0
	s_and_b64 s[2:3], s[2:3], s[4:5]
	v_readlane_b32 s86, v254, 50
	s_andn2_b64 vcc, exec, s[2:3]
	v_readlane_b32 s87, v254, 51
	s_cbranch_vccnz .LBB0_2997
	v_readlane_b32 s32, v254, 0
	s_nop 3
	s_bitcmp1_b32 s32, 3
	s_cbranch_scc0 .Lstag_3
	s_sleep 127
